# baseline (speedup 1.0000x reference)
.Lattn_after_rdv:
	s_cbranch_scc1 .Lattn_skip_tile
	ds_read_b128 v[46:49], v114
	ds_read_b128 v[42:45], v114 offset:2048
	ds_read_b128 v[102:105], v115
	ds_read_b128 v[38:41], v114 offset:4096
	ds_read_b128 v[106:109], v115 offset:2048
	ds_read_b128 v[34:37], v114 offset:6144
	ds_read_b128 v[110:113], v115 offset:4096
	ds_read_b128 v[76:79], v115 offset:6144
	s_cmp_lt_i32 s64, s79
	s_cbranch_scc1 .Lattn_do_dma
.Lattn_no_dma:
	s_add_i32 s48, s66, s64
	s_cmp_lg_u32 s48, 1
	s_waitcnt lgkmcnt(7)
	v_mfma_f32_16x16x32_f16 v[46:49], v[46:49], v[6:9], v[30:33]
	s_waitcnt lgkmcnt(6)
	v_mfma_f32_16x16x32_f16 v[42:45], v[42:45], v[6:9], v[30:33]
	s_waitcnt lgkmcnt(5)
	v_mfma_f32_16x16x32_f16 v[46:49], v[102:105], v[2:5], v[46:49]
	s_waitcnt lgkmcnt(4)
	v_mfma_f32_16x16x32_f16 v[38:41], v[38:41], v[6:9], v[30:33]
	s_waitcnt lgkmcnt(3)
	v_mfma_f32_16x16x32_f16 v[42:45], v[106:109], v[2:5], v[42:45]
	s_waitcnt lgkmcnt(2)
	v_mfma_f32_16x16x32_f16 v[34:37], v[34:37], v[6:9], v[30:33]
	s_waitcnt lgkmcnt(1)
	v_mfma_f32_16x16x32_f16 v[38:41], v[110:113], v[2:5], v[38:41]
	s_waitcnt lgkmcnt(0)
	v_mfma_f32_16x16x32_f16 v[34:37], v[76:79], v[2:5], v[34:37]
	s_cbranch_scc1 .LBB2_12
	v_cndmask_b32_e64 v69, v46, v100, s[2:3]
	v_cndmask_b32_e64 v46, v69, v46, s[4:5]
	v_cndmask_b32_e64 v47, v100, v47, s[4:5]
	v_cndmask_b32_e64 v48, v48, v100, s[6:7]
	v_cndmask_b32_e64 v49, v49, v100, s[8:9]
	v_cndmask_b32_e64 v42, v42, v100, s[10:11]
	v_cndmask_b32_e64 v43, v43, v100, s[12:13]
	v_cndmask_b32_e64 v44, v44, v100, s[14:15]
	v_cndmask_b32_e64 v45, v45, v100, s[16:17]
	v_cndmask_b32_e64 v38, v38, v100, s[18:19]
	v_cndmask_b32_e64 v39, v39, v100, s[20:21]
	v_cndmask_b32_e64 v40, v40, v100, s[22:23]
	v_cndmask_b32_e64 v41, v41, v100, s[24:25]
	v_cndmask_b32_e64 v34, v34, v100, s[26:27]
	v_cndmask_b32_e64 v35, v35, v100, s[28:29]
	v_cndmask_b32_e64 v36, v36, v100, s[30:31]
	v_cndmask_b32_e64 v37, v37, v100, s[34:35]
